# peel + nt + relaxed first two vmcnt waits of the up-proj K-loop for units after the first (epilogue stores no longer drained at unit start)
# baseline (speedup 1.0000x reference)
.LBB0_1172:
	s_ashr_i32 s39, s38, 31
	s_lshl_b64 s[4:5], s[38:39], 20
	s_add_u32 s40, s18, s4
	s_addc_u32 s41, s19, s5
	s_and_b64 s[4:5], s[36:37], exec
	s_cselect_b32 s4, s41, s1
	s_cselect_b32 s5, s40, s0
	s_ashr_i32 s35, s34, 31
	s_lshl_b64 s[42:43], s[34:35], 20
	s_add_u32 s42, s16, s42
	s_addc_u32 s43, s17, s43
	s_and_b64 s[48:49], s[36:37], exec
	s_cselect_b32 s35, s43, s47
	s_cselect_b32 s39, s42, s46
	s_add_u32 s76, s46, 0x10000
	s_addc_u32 s77, s47, 0
	s_mov_b32 s78, -2
	v_add_u32_e32 v124, s28, v156
	v_add_u32_e32 v170, s45, v156
	ds_read_b128 v[108:111], v124
	ds_read_b128 v[112:115], v124 offset:1024
	ds_read_b128 v[120:123], v124 offset:2048
	ds_read_b128 v[124:127], v124 offset:3072
	ds_read_b128 v[158:161], v170
	ds_read_b128 v[162:165], v170 offset:1024
	ds_read_b128 v[166:169], v170 offset:2048
	ds_read_b128 v[170:173], v170 offset:3072
	s_add_u32 s46, s0, 0x10000
	s_addc_u32 s47, s1, 0
	s_cmp_eq_u32 s78, 28
	s_cselect_b32 s52, s5, s46
	s_cselect_b32 s53, s4, s47
	s_cselect_b32 s50, s39, s76
	s_cselect_b32 s51, s35, s77
	s_add_u32 s48, s52, 0x8000
	s_addc_u32 s49, s53, 0
	v_lshl_add_u64 v[206:207], s[0:1], 0, v[152:153]
	s_add_i32 m0, s56, 0xc000
	ds_read_b128 v[174:177], v157
	ds_read_b128 v[178:181], v157 offset:1024
	ds_read_b128 v[182:185], v157 offset:2048
	ds_read_b128 v[186:189], v157 offset:3072
	ds_read_b128 v[190:193], v157 offset:4096
	ds_read_b128 v[194:197], v157 offset:5120
	ds_read_b128 v[198:201], v157 offset:6144
	ds_read_b128 v[202:205], v157 offset:7168
	global_load_lds_dwordx4 v[206:207], off
	v_lshl_add_u64 v[206:207], s[0:1], 0, v[154:155]
	s_add_i32 m0, s56, 0xe000
	s_nop 0
	global_load_lds_dwordx4 v[206:207], off
	s_cmp_eq_u32 s75, 0
	s_cbranch_scc1 .Lupw_norm_0
	s_waitcnt vmcnt(24)
	s_branch .Lupw_join_0
.Lupw_norm_0:
	s_waitcnt vmcnt(8)
.Lupw_join_0:
	s_waitcnt lgkmcnt(0)
	s_barrier
	s_setprio 1
	s_waitcnt lgkmcnt(0)
	v_mfma_f32_16x16x32_bf16 v[140:143], v[108:111], v[174:177], 0
	v_mfma_f32_16x16x32_bf16 v[136:139], v[120:123], v[174:177], 0
	v_mfma_f32_16x16x32_bf16 v[116:119], v[108:111], v[182:185], 0
	v_mfma_f32_16x16x32_bf16 v[104:107], v[120:123], v[182:185], 0
	v_mfma_f32_16x16x32_bf16 v[92:95], v[108:111], v[190:193], 0
	v_mfma_f32_16x16x32_bf16 v[88:91], v[120:123], v[190:193], 0
	v_mfma_f32_16x16x32_bf16 v[76:79], v[108:111], v[198:201], 0
	v_mfma_f32_16x16x32_bf16 v[72:75], v[120:123], v[198:201], 0
	v_mfma_f32_16x16x32_bf16 v[140:143], v[112:115], v[178:181], v[140:143]
	v_mfma_f32_16x16x32_bf16 v[136:139], v[124:127], v[178:181], v[136:139]
	v_mfma_f32_16x16x32_bf16 v[116:119], v[112:115], v[186:189], v[116:119]
	v_mfma_f32_16x16x32_bf16 v[104:107], v[124:127], v[186:189], v[104:107]
	v_mfma_f32_16x16x32_bf16 v[92:95], v[112:115], v[194:197], v[92:95]
	v_mfma_f32_16x16x32_bf16 v[88:91], v[124:127], v[194:197], v[88:91]
	v_mfma_f32_16x16x32_bf16 v[76:79], v[112:115], v[202:205], v[76:79]
	v_mfma_f32_16x16x32_bf16 v[72:75], v[124:127], v[202:205], v[72:75]
	s_setprio 0
	s_setprio 1
	v_mfma_f32_16x16x32_bf16 v[132:135], v[158:161], v[174:177], 0
	v_mfma_f32_16x16x32_bf16 v[128:131], v[166:169], v[174:177], 0
	v_mfma_f32_16x16x32_bf16 v[100:103], v[158:161], v[182:185], 0
	v_mfma_f32_16x16x32_bf16 v[96:99], v[166:169], v[182:185], 0
	v_mfma_f32_16x16x32_bf16 v[84:87], v[158:161], v[190:193], 0
	v_mfma_f32_16x16x32_bf16 v[80:83], v[166:169], v[190:193], 0
	v_mfma_f32_16x16x32_bf16 v[68:71], v[158:161], v[198:201], 0
	v_mfma_f32_16x16x32_bf16 v[64:67], v[166:169], v[198:201], 0
	v_mfma_f32_16x16x32_bf16 v[132:135], v[162:165], v[178:181], v[132:135]
	v_mfma_f32_16x16x32_bf16 v[128:131], v[170:173], v[178:181], v[128:131]
	v_mfma_f32_16x16x32_bf16 v[100:103], v[162:165], v[186:189], v[100:103]
	v_mfma_f32_16x16x32_bf16 v[96:99], v[170:173], v[186:189], v[96:99]
	v_mfma_f32_16x16x32_bf16 v[84:87], v[162:165], v[194:197], v[84:87]
	v_mfma_f32_16x16x32_bf16 v[80:83], v[170:173], v[194:197], v[80:83]
	v_mfma_f32_16x16x32_bf16 v[68:71], v[162:165], v[202:205], v[68:71]
	v_mfma_f32_16x16x32_bf16 v[64:67], v[170:173], v[202:205], v[64:67]
	s_setprio 0
	s_barrier
	s_mov_b32 m0, s30
	v_lshl_add_u64 v[206:207], s[50:51], 0, v[146:147]
	s_add_u32 s0, s50, 0x4000
	ds_read_b128 v[174:177], v157 offset:16384
	ds_read_b128 v[178:181], v157 offset:17408
	ds_read_b128 v[182:185], v157 offset:18432
	ds_read_b128 v[186:189], v157 offset:19456
	ds_read_b128 v[190:193], v157 offset:20480
	ds_read_b128 v[194:197], v157 offset:21504
	ds_read_b128 v[198:201], v157 offset:22528
	ds_read_b128 v[202:205], v157 offset:23552
	global_load_lds_dwordx4 v[206:207], off
	v_lshl_add_u64 v[206:207], s[50:51], 0, v[150:151]
	s_mov_b32 m0, s31
	s_addc_u32 s1, s51, 0
	global_load_lds_dwordx4 v[206:207], off
	v_lshl_add_u64 v[206:207], s[0:1], 0, v[146:147]
	s_mov_b32 m0, s54
	s_nop 0
	global_load_lds_dwordx4 v[206:207], off
	v_lshl_add_u64 v[206:207], s[0:1], 0, v[150:151]
	s_mov_b32 m0, s55
	s_nop 0
	global_load_lds_dwordx4 v[206:207], off
	v_lshl_add_u64 v[206:207], s[52:53], 0, v[144:145]
	s_mov_b32 m0, s56
	s_nop 0
	global_load_lds_dwordx4 v[206:207], off
	v_lshl_add_u64 v[206:207], s[52:53], 0, v[148:149]
	s_mov_b32 m0, s57
	s_nop 0
	global_load_lds_dwordx4 v[206:207], off
	s_cmp_eq_u32 s75, 0
	s_cbranch_scc1 .Lupw_norm_1
	s_waitcnt vmcnt(24)
	s_branch .Lupw_join_1

.Lupw_join_1:
	s_waitcnt lgkmcnt(0)
	s_barrier
	s_setprio 1
	s_waitcnt lgkmcnt(0)
	v_mfma_f32_16x16x32_bf16 v[60:63], v[108:111], v[174:177], 0
	v_mfma_f32_16x16x32_bf16 v[56:59], v[120:123], v[174:177], 0
	v_mfma_f32_16x16x32_bf16 v[44:47], v[108:111], v[182:185], 0
	v_mfma_f32_16x16x32_bf16 v[40:43], v[120:123], v[182:185], 0
	v_mfma_f32_16x16x32_bf16 v[28:31], v[108:111], v[190:193], 0
	v_mfma_f32_16x16x32_bf16 v[24:27], v[120:123], v[190:193], 0
	v_mfma_f32_16x16x32_bf16 v[12:15], v[108:111], v[198:201], 0
	v_mfma_f32_16x16x32_bf16 v[8:11], v[120:123], v[198:201], 0
	v_mfma_f32_16x16x32_bf16 v[60:63], v[112:115], v[178:181], v[60:63]
	v_mfma_f32_16x16x32_bf16 v[56:59], v[124:127], v[178:181], v[56:59]
	v_mfma_f32_16x16x32_bf16 v[44:47], v[112:115], v[186:189], v[44:47]
	v_mfma_f32_16x16x32_bf16 v[40:43], v[124:127], v[186:189], v[40:43]
	v_mfma_f32_16x16x32_bf16 v[28:31], v[112:115], v[194:197], v[28:31]
	v_mfma_f32_16x16x32_bf16 v[24:27], v[124:127], v[194:197], v[24:27]
	v_mfma_f32_16x16x32_bf16 v[12:15], v[112:115], v[202:205], v[12:15]
	v_mfma_f32_16x16x32_bf16 v[8:11], v[124:127], v[202:205], v[8:11]
	s_setprio 0
	s_setprio 1
	v_mfma_f32_16x16x32_bf16 v[52:55], v[158:161], v[174:177], 0
	v_mfma_f32_16x16x32_bf16 v[48:51], v[166:169], v[174:177], 0
	v_mfma_f32_16x16x32_bf16 v[36:39], v[158:161], v[182:185], 0
	v_mfma_f32_16x16x32_bf16 v[32:35], v[166:169], v[182:185], 0
	v_mfma_f32_16x16x32_bf16 v[20:23], v[158:161], v[190:193], 0
	v_mfma_f32_16x16x32_bf16 v[16:19], v[166:169], v[190:193], 0
	v_mfma_f32_16x16x32_bf16 v[4:7], v[158:161], v[198:201], 0
	v_mfma_f32_16x16x32_bf16 v[0:3], v[166:169], v[198:201], 0
	v_mfma_f32_16x16x32_bf16 v[52:55], v[162:165], v[178:181], v[52:55]
	v_mfma_f32_16x16x32_bf16 v[48:51], v[170:173], v[178:181], v[48:51]
	v_mfma_f32_16x16x32_bf16 v[36:39], v[162:165], v[186:189], v[36:39]
	v_mfma_f32_16x16x32_bf16 v[32:35], v[170:173], v[186:189], v[32:35]
	v_mfma_f32_16x16x32_bf16 v[20:23], v[162:165], v[194:197], v[20:23]
	v_mfma_f32_16x16x32_bf16 v[16:19], v[170:173], v[194:197], v[16:19]
	v_mfma_f32_16x16x32_bf16 v[4:7], v[162:165], v[202:205], v[4:7]
	v_mfma_f32_16x16x32_bf16 v[0:3], v[170:173], v[202:205], v[0:3]
	s_setprio 0
	s_barrier
	v_add_u32_e32 v124, s62, v156
	v_add_u32_e32 v170, s67, v156
	ds_read_b128 v[108:111], v124
	ds_read_b128 v[112:115], v124 offset:1024
	ds_read_b128 v[120:123], v124 offset:2048
	ds_read_b128 v[124:127], v124 offset:3072
	ds_read_b128 v[158:161], v170
	ds_read_b128 v[162:165], v170 offset:1024
	ds_read_b128 v[166:169], v170 offset:2048
	ds_read_b128 v[170:173], v170 offset:3072
	s_add_u32 s0, s52, 0x4000
	s_addc_u32 s1, s53, 0
	s_mov_b32 m0, s58
	v_lshl_add_u64 v[206:207], s[0:1], 0, v[144:145]
	ds_read_b128 v[174:177], v157 offset:32768
	ds_read_b128 v[178:181], v157 offset:33792
	ds_read_b128 v[182:185], v157 offset:34816
	ds_read_b128 v[186:189], v157 offset:35840
	ds_read_b128 v[190:193], v157 offset:36864
	ds_read_b128 v[194:197], v157 offset:37888
	ds_read_b128 v[198:201], v157 offset:38912
	ds_read_b128 v[202:205], v157 offset:39936
	global_load_lds_dwordx4 v[206:207], off
	v_lshl_add_u64 v[206:207], s[0:1], 0, v[148:149]
	s_mov_b32 m0, s59
	s_nop 0
	global_load_lds_dwordx4 v[206:207], off
	s_waitcnt vmcnt(8)
	s_waitcnt lgkmcnt(0)
	s_barrier
	s_setprio 1
	s_waitcnt lgkmcnt(0)
	v_mfma_f32_16x16x32_bf16 v[140:143], v[108:111], v[174:177], v[140:143]
	v_mfma_f32_16x16x32_bf16 v[136:139], v[120:123], v[174:177], v[136:139]
	v_mfma_f32_16x16x32_bf16 v[116:119], v[108:111], v[182:185], v[116:119]
	v_mfma_f32_16x16x32_bf16 v[104:107], v[120:123], v[182:185], v[104:107]
	v_mfma_f32_16x16x32_bf16 v[92:95], v[108:111], v[190:193], v[92:95]
	v_mfma_f32_16x16x32_bf16 v[88:91], v[120:123], v[190:193], v[88:91]
	v_mfma_f32_16x16x32_bf16 v[76:79], v[108:111], v[198:201], v[76:79]
	v_mfma_f32_16x16x32_bf16 v[72:75], v[120:123], v[198:201], v[72:75]
	v_mfma_f32_16x16x32_bf16 v[140:143], v[112:115], v[178:181], v[140:143]
	v_mfma_f32_16x16x32_bf16 v[136:139], v[124:127], v[178:181], v[136:139]
	v_mfma_f32_16x16x32_bf16 v[116:119], v[112:115], v[186:189], v[116:119]
	v_mfma_f32_16x16x32_bf16 v[104:107], v[124:127], v[186:189], v[104:107]
	v_mfma_f32_16x16x32_bf16 v[92:95], v[112:115], v[194:197], v[92:95]
	v_mfma_f32_16x16x32_bf16 v[88:91], v[124:127], v[194:197], v[88:91]
	v_mfma_f32_16x16x32_bf16 v[76:79], v[112:115], v[202:205], v[76:79]
	v_mfma_f32_16x16x32_bf16 v[72:75], v[124:127], v[202:205], v[72:75]
	s_setprio 0
	s_setprio 1
	v_mfma_f32_16x16x32_bf16 v[132:135], v[158:161], v[174:177], v[132:135]
	v_mfma_f32_16x16x32_bf16 v[128:131], v[166:169], v[174:177], v[128:131]
	v_mfma_f32_16x16x32_bf16 v[100:103], v[158:161], v[182:185], v[100:103]
	v_mfma_f32_16x16x32_bf16 v[96:99], v[166:169], v[182:185], v[96:99]
	v_mfma_f32_16x16x32_bf16 v[84:87], v[158:161], v[190:193], v[84:87]
	v_mfma_f32_16x16x32_bf16 v[80:83], v[166:169], v[190:193], v[80:83]
	v_mfma_f32_16x16x32_bf16 v[68:71], v[158:161], v[198:201], v[68:71]
	v_mfma_f32_16x16x32_bf16 v[64:67], v[166:169], v[198:201], v[64:67]
	v_mfma_f32_16x16x32_bf16 v[132:135], v[162:165], v[178:181], v[132:135]
	v_mfma_f32_16x16x32_bf16 v[128:131], v[170:173], v[178:181], v[128:131]
	v_mfma_f32_16x16x32_bf16 v[100:103], v[162:165], v[186:189], v[100:103]
	v_mfma_f32_16x16x32_bf16 v[96:99], v[170:173], v[186:189], v[96:99]
	v_mfma_f32_16x16x32_bf16 v[84:87], v[162:165], v[194:197], v[84:87]
	v_mfma_f32_16x16x32_bf16 v[80:83], v[170:173], v[194:197], v[80:83]
	v_mfma_f32_16x16x32_bf16 v[68:71], v[162:165], v[202:205], v[68:71]
	v_mfma_f32_16x16x32_bf16 v[64:67], v[170:173], v[202:205], v[64:67]
	s_setprio 0
	s_barrier
	s_add_u32 s0, s50, 0x8000
	s_addc_u32 s1, s51, 0
	s_mov_b32 m0, s63
	v_lshl_add_u64 v[206:207], s[0:1], 0, v[146:147]
	ds_read_b128 v[174:177], v157 offset:49152
	ds_read_b128 v[178:181], v157 offset:50176
	ds_read_b128 v[182:185], v157 offset:51200
	ds_read_b128 v[186:189], v157 offset:52224
	ds_read_b128 v[190:193], v157 offset:53248
	ds_read_b128 v[194:197], v157 offset:54272
	ds_read_b128 v[198:201], v157 offset:55296
	ds_read_b128 v[202:205], v157 offset:56320
	global_load_lds_dwordx4 v[206:207], off
	v_lshl_add_u64 v[206:207], s[0:1], 0, v[150:151]
	s_add_u32 s0, s50, 0xc000
	s_mov_b32 m0, s64
	s_addc_u32 s1, s51, 0
	global_load_lds_dwordx4 v[206:207], off
	v_lshl_add_u64 v[206:207], s[0:1], 0, v[146:147]
	s_mov_b32 m0, s68
	s_nop 0
	global_load_lds_dwordx4 v[206:207], off
	v_lshl_add_u64 v[206:207], s[0:1], 0, v[150:151]
	s_mov_b32 m0, s69
	s_nop 0
	global_load_lds_dwordx4 v[206:207], off
	v_lshl_add_u64 v[206:207], s[48:49], 0, v[144:145]
	s_mov_b32 m0, s65
	s_nop 0
	global_load_lds_dwordx4 v[206:207], off
	v_lshl_add_u64 v[206:207], s[48:49], 0, v[148:149]
	s_mov_b32 m0, s66
	s_nop 0
	global_load_lds_dwordx4 v[206:207], off
	s_waitcnt vmcnt(8)
	s_waitcnt lgkmcnt(0)
	s_barrier
	s_setprio 1
	s_waitcnt lgkmcnt(0)
	v_mfma_f32_16x16x32_bf16 v[60:63], v[108:111], v[174:177], v[60:63]
	v_mfma_f32_16x16x32_bf16 v[56:59], v[120:123], v[174:177], v[56:59]
	v_mfma_f32_16x16x32_bf16 v[44:47], v[108:111], v[182:185], v[44:47]
	v_mfma_f32_16x16x32_bf16 v[40:43], v[120:123], v[182:185], v[40:43]
	v_mfma_f32_16x16x32_bf16 v[28:31], v[108:111], v[190:193], v[28:31]
	v_mfma_f32_16x16x32_bf16 v[24:27], v[120:123], v[190:193], v[24:27]
	v_mfma_f32_16x16x32_bf16 v[12:15], v[108:111], v[198:201], v[12:15]
	v_mfma_f32_16x16x32_bf16 v[8:11], v[120:123], v[198:201], v[8:11]
	v_mfma_f32_16x16x32_bf16 v[60:63], v[112:115], v[178:181], v[60:63]
	v_mfma_f32_16x16x32_bf16 v[56:59], v[124:127], v[178:181], v[56:59]
	v_mfma_f32_16x16x32_bf16 v[44:47], v[112:115], v[186:189], v[44:47]
	v_mfma_f32_16x16x32_bf16 v[40:43], v[124:127], v[186:189], v[40:43]
	v_mfma_f32_16x16x32_bf16 v[28:31], v[112:115], v[194:197], v[28:31]
	v_mfma_f32_16x16x32_bf16 v[24:27], v[124:127], v[194:197], v[24:27]
	v_mfma_f32_16x16x32_bf16 v[12:15], v[112:115], v[202:205], v[12:15]
	v_mfma_f32_16x16x32_bf16 v[8:11], v[124:127], v[202:205], v[8:11]
	s_setprio 0
	s_setprio 1
	v_mfma_f32_16x16x32_bf16 v[52:55], v[158:161], v[174:177], v[52:55]
	v_mfma_f32_16x16x32_bf16 v[48:51], v[166:169], v[174:177], v[48:51]
	v_mfma_f32_16x16x32_bf16 v[36:39], v[158:161], v[182:185], v[36:39]
	v_mfma_f32_16x16x32_bf16 v[32:35], v[166:169], v[182:185], v[32:35]
	v_mfma_f32_16x16x32_bf16 v[20:23], v[158:161], v[190:193], v[20:23]
	v_mfma_f32_16x16x32_bf16 v[16:19], v[166:169], v[190:193], v[16:19]
	v_mfma_f32_16x16x32_bf16 v[4:7], v[158:161], v[198:201], v[4:7]
	v_mfma_f32_16x16x32_bf16 v[0:3], v[166:169], v[198:201], v[0:3]
	v_mfma_f32_16x16x32_bf16 v[52:55], v[162:165], v[178:181], v[52:55]
	v_mfma_f32_16x16x32_bf16 v[48:51], v[170:173], v[178:181], v[48:51]
	v_mfma_f32_16x16x32_bf16 v[36:39], v[162:165], v[186:189], v[36:39]
	v_mfma_f32_16x16x32_bf16 v[32:35], v[170:173], v[186:189], v[32:35]
	v_mfma_f32_16x16x32_bf16 v[20:23], v[162:165], v[194:197], v[20:23]
	v_mfma_f32_16x16x32_bf16 v[16:19], v[170:173], v[194:197], v[16:19]
	v_mfma_f32_16x16x32_bf16 v[4:7], v[162:165], v[202:205], v[4:7]
	v_mfma_f32_16x16x32_bf16 v[0:3], v[170:173], v[202:205], v[0:3]
	s_setprio 0
	s_barrier
	s_add_i32 s78, s78, 2
	s_add_u32 s76, s76, 0x10000
	s_addc_u32 s77, s77, 0
	s_cmp_gt_u32 s78, 29
	s_mov_b64 s[0:1], s[46:47]
